# speedup vs baseline: 1.0101x; 1.0052x over previous
.LBB5_9:
	ds_read_b128 v[168:171], v165
	ds_read_b128 v[172:175], v165 offset:1024
	ds_read_b128 v[176:179], v165 offset:2048
	ds_read_b128 v[192:195], v165 offset:3072
	s_mov_b32 m0, s80
	s_add_u32 s100, s96, s0
	s_addc_u32 s101, s97, s1
	global_load_lds_dwordx4 v254, s[100:101]
	s_mov_b32 m0, s81
	s_nop 0
	global_load_lds_dwordx4 v255, s[100:101]
	ds_read_b128 v[196:199], v150
	ds_read_b128 v[200:203], v150 offset:1024
	ds_read_b128 v[204:207], v149
	ds_read_b128 v[208:211], v149 offset:1024
	ds_read_b128 v[212:215], v148
	ds_read_b128 v[216:219], v148 offset:1024
	ds_read_b128 v[220:223], v147
	ds_read_b128 v[224:227], v147 offset:1024
	s_waitcnt lgkmcnt(8)
	s_barrier
	s_waitcnt lgkmcnt(0)
	s_setprio 1
	s_waitcnt lgkmcnt(0)
	v_mfma_f32_16x16x32_f16 v[126:129], v[168:171], v[196:199], v[126:129]
	v_mfma_f32_16x16x32_f16 v[122:125], v[176:179], v[196:199], v[122:125]
	v_mfma_f32_16x16x32_f16 v[118:121], v[168:171], v[204:207], v[118:121]
	v_mfma_f32_16x16x32_f16 v[114:117], v[176:179], v[204:207], v[114:117]
	v_mfma_f32_16x16x32_f16 v[110:113], v[168:171], v[212:215], v[110:113]
	v_mfma_f32_16x16x32_f16 v[106:109], v[176:179], v[212:215], v[106:109]
	v_mfma_f32_16x16x32_f16 v[102:105], v[168:171], v[220:223], v[102:105]
	v_mfma_f32_16x16x32_f16 v[98:101], v[176:179], v[220:223], v[98:101]
	v_mfma_f32_16x16x32_f16 v[126:129], v[172:175], v[200:203], v[126:129]
	v_mfma_f32_16x16x32_f16 v[122:125], v[192:195], v[200:203], v[122:125]
	v_mfma_f32_16x16x32_f16 v[118:121], v[172:175], v[208:211], v[118:121]
	v_mfma_f32_16x16x32_f16 v[114:117], v[192:195], v[208:211], v[114:117]
	v_mfma_f32_16x16x32_f16 v[110:113], v[172:175], v[216:219], v[110:113]
	v_mfma_f32_16x16x32_f16 v[106:109], v[192:195], v[216:219], v[106:109]
	v_mfma_f32_16x16x32_f16 v[102:105], v[172:175], v[224:227], v[102:105]
	v_mfma_f32_16x16x32_f16 v[98:101], v[192:195], v[224:227], v[98:101]
	s_setprio 0
	s_barrier
	s_mov_b32 m0, s82
	ds_read_b128 v[228:231], v163
	ds_read_b128 v[232:235], v163 offset:1024
	ds_read_b128 v[236:239], v163 offset:2048
	ds_read_b128 v[240:243], v163 offset:3072
	s_add_u32 s100, s98, s28
	s_addc_u32 s101, s99, s29
	global_load_lds_dwordx4 v254, s[100:101]
	s_mov_b32 m0, s83
	s_nop 0
	global_load_lds_dwordx4 v255, s[100:101]
	s_barrier
	s_waitcnt lgkmcnt(0)
	s_setprio 1
	s_waitcnt lgkmcnt(0)
	v_mfma_f32_16x16x32_f16 v[94:97], v[228:231], v[196:199], v[94:97]
	v_mfma_f32_16x16x32_f16 v[90:93], v[236:239], v[196:199], v[90:93]
	v_mfma_f32_16x16x32_f16 v[86:89], v[228:231], v[204:207], v[86:89]
	v_mfma_f32_16x16x32_f16 v[82:85], v[236:239], v[204:207], v[82:85]
	v_mfma_f32_16x16x32_f16 v[78:81], v[228:231], v[212:215], v[78:81]
	v_mfma_f32_16x16x32_f16 v[74:77], v[236:239], v[212:215], v[74:77]
	v_mfma_f32_16x16x32_f16 v[70:73], v[228:231], v[220:223], v[70:73]
	v_mfma_f32_16x16x32_f16 v[66:69], v[236:239], v[220:223], v[66:69]
	v_mfma_f32_16x16x32_f16 v[94:97], v[232:235], v[200:203], v[94:97]
	v_mfma_f32_16x16x32_f16 v[90:93], v[240:243], v[200:203], v[90:93]
	v_mfma_f32_16x16x32_f16 v[86:89], v[232:235], v[208:211], v[86:89]
	v_mfma_f32_16x16x32_f16 v[82:85], v[240:243], v[208:211], v[82:85]
	v_mfma_f32_16x16x32_f16 v[78:81], v[232:235], v[216:219], v[78:81]
	v_mfma_f32_16x16x32_f16 v[74:77], v[240:243], v[216:219], v[74:77]
	v_mfma_f32_16x16x32_f16 v[70:73], v[232:235], v[224:227], v[70:73]
	v_mfma_f32_16x16x32_f16 v[66:69], v[240:243], v[224:227], v[66:69]
	s_setprio 0
	s_mov_b32 m0, s84
	s_barrier
	ds_read_b128 v[196:199], v150 offset:16384
	ds_read_b128 v[200:203], v150 offset:17408
	ds_read_b128 v[204:207], v149 offset:16384
	ds_read_b128 v[208:211], v149 offset:17408
	ds_read_b128 v[212:215], v148 offset:16384
	ds_read_b128 v[216:219], v148 offset:17408
	ds_read_b128 v[220:223], v147 offset:16384
	ds_read_b128 v[224:227], v147 offset:17408
	s_add_u32 s100, s96, s28
	s_addc_u32 s101, s97, s29
	global_load_lds_dwordx4 v254, s[100:101]
	s_mov_b32 m0, s85
	s_nop 0
	global_load_lds_dwordx4 v255, s[100:101]
	s_barrier
	s_waitcnt lgkmcnt(0)
	s_setprio 1
	s_waitcnt lgkmcnt(0)
	v_mfma_f32_16x16x32_f16 v[62:65], v[168:171], v[196:199], v[62:65]
	v_mfma_f32_16x16x32_f16 v[58:61], v[176:179], v[196:199], v[58:61]
	v_mfma_f32_16x16x32_f16 v[54:57], v[168:171], v[204:207], v[54:57]
	v_mfma_f32_16x16x32_f16 v[50:53], v[176:179], v[204:207], v[50:53]
	v_mfma_f32_16x16x32_f16 v[46:49], v[168:171], v[212:215], v[46:49]
	v_mfma_f32_16x16x32_f16 v[42:45], v[176:179], v[212:215], v[42:45]
	v_mfma_f32_16x16x32_f16 v[38:41], v[168:171], v[220:223], v[38:41]
	v_mfma_f32_16x16x32_f16 v[34:37], v[176:179], v[220:223], v[34:37]
	v_mfma_f32_16x16x32_f16 v[62:65], v[172:175], v[200:203], v[62:65]
	v_mfma_f32_16x16x32_f16 v[58:61], v[192:195], v[200:203], v[58:61]
	v_mfma_f32_16x16x32_f16 v[54:57], v[172:175], v[208:211], v[54:57]
	v_mfma_f32_16x16x32_f16 v[50:53], v[192:195], v[208:211], v[50:53]
	v_mfma_f32_16x16x32_f16 v[46:49], v[172:175], v[216:219], v[46:49]
	v_mfma_f32_16x16x32_f16 v[42:45], v[192:195], v[216:219], v[42:45]
	v_mfma_f32_16x16x32_f16 v[38:41], v[172:175], v[224:227], v[38:41]
	v_mfma_f32_16x16x32_f16 v[34:37], v[192:195], v[224:227], v[34:37]
	s_setprio 0
	s_barrier
	s_mov_b32 m0, s86
	s_add_u32 s100, s98, s30
	s_addc_u32 s101, s99, s31
	global_load_lds_dwordx4 v254, s[100:101]
	s_mov_b32 m0, s87
	s_nop 0
	global_load_lds_dwordx4 v255, s[100:101]
	s_waitcnt vmcnt(6)
	s_barrier
	s_setprio 1
	v_mfma_f32_16x16x32_f16 v[30:33], v[228:231], v[196:199], v[30:33]
	v_mfma_f32_16x16x32_f16 v[26:29], v[236:239], v[196:199], v[26:29]
	v_mfma_f32_16x16x32_f16 v[22:25], v[228:231], v[204:207], v[22:25]
	v_mfma_f32_16x16x32_f16 v[18:21], v[236:239], v[204:207], v[18:21]
	v_mfma_f32_16x16x32_f16 v[14:17], v[228:231], v[212:215], v[14:17]
	v_mfma_f32_16x16x32_f16 v[10:13], v[236:239], v[212:215], v[10:13]
	v_mfma_f32_16x16x32_f16 v[6:9], v[228:231], v[220:223], v[6:9]
	v_mfma_f32_16x16x32_f16 v[2:5], v[236:239], v[220:223], v[2:5]
	v_mfma_f32_16x16x32_f16 v[30:33], v[232:235], v[200:203], v[30:33]
	v_mfma_f32_16x16x32_f16 v[26:29], v[240:243], v[200:203], v[26:29]
	v_mfma_f32_16x16x32_f16 v[22:25], v[232:235], v[208:211], v[22:25]
	v_mfma_f32_16x16x32_f16 v[18:21], v[240:243], v[208:211], v[18:21]
	v_mfma_f32_16x16x32_f16 v[14:17], v[232:235], v[216:219], v[14:17]
	v_mfma_f32_16x16x32_f16 v[10:13], v[240:243], v[216:219], v[10:13]
	v_mfma_f32_16x16x32_f16 v[6:9], v[232:235], v[224:227], v[6:9]
	v_mfma_f32_16x16x32_f16 v[2:5], v[240:243], v[224:227], v[2:5]
	s_setprio 0
	s_barrier
	ds_read_b128 v[168:171], v133
	ds_read_b128 v[172:175], v133 offset:1024
	ds_read_b128 v[176:179], v133 offset:2048
	ds_read_b128 v[192:195], v133 offset:3072
	s_mov_b32 m0, s88
	ds_read_b128 v[196:199], v150 offset:32768
	ds_read_b128 v[200:203], v150 offset:33792
	ds_read_b128 v[204:207], v149 offset:32768
	ds_read_b128 v[208:211], v149 offset:33792
	ds_read_b128 v[212:215], v148 offset:32768
	ds_read_b128 v[216:219], v148 offset:33792
	ds_read_b128 v[220:223], v147 offset:32768
	ds_read_b128 v[224:227], v147 offset:33792
	s_add_u32 s100, s96, s30
	s_addc_u32 s101, s97, s31
	global_load_lds_dwordx4 v254, s[100:101]
	s_mov_b32 m0, s89
	s_nop 0
	global_load_lds_dwordx4 v255, s[100:101]
	s_waitcnt lgkmcnt(8)
	s_barrier
	s_waitcnt lgkmcnt(0)
	s_setprio 1
	s_waitcnt lgkmcnt(0)
	v_mfma_f32_16x16x32_f16 v[126:129], v[168:171], v[196:199], v[126:129]
	v_mfma_f32_16x16x32_f16 v[122:125], v[176:179], v[196:199], v[122:125]
	v_mfma_f32_16x16x32_f16 v[118:121], v[168:171], v[204:207], v[118:121]
	v_mfma_f32_16x16x32_f16 v[114:117], v[176:179], v[204:207], v[114:117]
	v_mfma_f32_16x16x32_f16 v[110:113], v[168:171], v[212:215], v[110:113]
	v_mfma_f32_16x16x32_f16 v[106:109], v[176:179], v[212:215], v[106:109]
	v_mfma_f32_16x16x32_f16 v[102:105], v[168:171], v[220:223], v[102:105]
	v_mfma_f32_16x16x32_f16 v[98:101], v[176:179], v[220:223], v[98:101]
	v_mfma_f32_16x16x32_f16 v[126:129], v[172:175], v[200:203], v[126:129]
	v_mfma_f32_16x16x32_f16 v[122:125], v[192:195], v[200:203], v[122:125]
	v_mfma_f32_16x16x32_f16 v[118:121], v[172:175], v[208:211], v[118:121]
	v_mfma_f32_16x16x32_f16 v[114:117], v[192:195], v[208:211], v[114:117]
	v_mfma_f32_16x16x32_f16 v[110:113], v[172:175], v[216:219], v[110:113]
	v_mfma_f32_16x16x32_f16 v[106:109], v[192:195], v[216:219], v[106:109]
	v_mfma_f32_16x16x32_f16 v[102:105], v[172:175], v[224:227], v[102:105]
	v_mfma_f32_16x16x32_f16 v[98:101], v[192:195], v[224:227], v[98:101]
	s_setprio 0
	s_barrier
	s_mov_b32 m0, s90
	ds_read_b128 v[228:231], v131
	ds_read_b128 v[232:235], v131 offset:1024
	ds_read_b128 v[236:239], v131 offset:2048
	ds_read_b128 v[240:243], v131 offset:3072
	s_add_u32 s100, s98, s52
	s_addc_u32 s101, s99, s53
	global_load_lds_dwordx4 v254, s[100:101]
	s_mov_b32 m0, s91
	s_nop 0
	global_load_lds_dwordx4 v255, s[100:101]
	s_barrier
	s_waitcnt lgkmcnt(0)
	s_setprio 1
	s_waitcnt lgkmcnt(0)
	v_mfma_f32_16x16x32_f16 v[94:97], v[228:231], v[196:199], v[94:97]
	v_mfma_f32_16x16x32_f16 v[90:93], v[236:239], v[196:199], v[90:93]
	v_mfma_f32_16x16x32_f16 v[86:89], v[228:231], v[204:207], v[86:89]
	v_mfma_f32_16x16x32_f16 v[82:85], v[236:239], v[204:207], v[82:85]
	v_mfma_f32_16x16x32_f16 v[78:81], v[228:231], v[212:215], v[78:81]
	v_mfma_f32_16x16x32_f16 v[74:77], v[236:239], v[212:215], v[74:77]
	v_mfma_f32_16x16x32_f16 v[70:73], v[228:231], v[220:223], v[70:73]
	v_mfma_f32_16x16x32_f16 v[66:69], v[236:239], v[220:223], v[66:69]
	v_mfma_f32_16x16x32_f16 v[94:97], v[232:235], v[200:203], v[94:97]
	v_mfma_f32_16x16x32_f16 v[90:93], v[240:243], v[200:203], v[90:93]
	v_mfma_f32_16x16x32_f16 v[86:89], v[232:235], v[208:211], v[86:89]
	v_mfma_f32_16x16x32_f16 v[82:85], v[240:243], v[208:211], v[82:85]
	v_mfma_f32_16x16x32_f16 v[78:81], v[232:235], v[216:219], v[78:81]
	v_mfma_f32_16x16x32_f16 v[74:77], v[240:243], v[216:219], v[74:77]
	v_mfma_f32_16x16x32_f16 v[70:73], v[232:235], v[224:227], v[70:73]
	v_mfma_f32_16x16x32_f16 v[66:69], v[240:243], v[224:227], v[66:69]
	s_setprio 0
	s_mov_b32 m0, s92
	s_barrier
	ds_read_b128 v[196:199], v150 offset:49152
	ds_read_b128 v[200:203], v150 offset:50176
	ds_read_b128 v[204:207], v149 offset:49152
	ds_read_b128 v[208:211], v149 offset:50176
	ds_read_b128 v[212:215], v148 offset:49152
	ds_read_b128 v[216:219], v148 offset:50176
	ds_read_b128 v[220:223], v147 offset:49152
	ds_read_b128 v[224:227], v147 offset:50176
	s_add_u32 s100, s96, s52
	s_addc_u32 s101, s97, s53
	global_load_lds_dwordx4 v254, s[100:101]
	s_mov_b32 m0, s93
	s_nop 0
	global_load_lds_dwordx4 v255, s[100:101]
	s_barrier
	s_waitcnt lgkmcnt(0)
	s_setprio 1
	s_waitcnt lgkmcnt(0)
	v_mfma_f32_16x16x32_f16 v[62:65], v[168:171], v[196:199], v[62:65]
	v_mfma_f32_16x16x32_f16 v[58:61], v[176:179], v[196:199], v[58:61]
	v_mfma_f32_16x16x32_f16 v[54:57], v[168:171], v[204:207], v[54:57]
	v_mfma_f32_16x16x32_f16 v[50:53], v[176:179], v[204:207], v[50:53]
	v_mfma_f32_16x16x32_f16 v[46:49], v[168:171], v[212:215], v[46:49]
	v_mfma_f32_16x16x32_f16 v[42:45], v[176:179], v[212:215], v[42:45]
	v_mfma_f32_16x16x32_f16 v[38:41], v[168:171], v[220:223], v[38:41]
	v_mfma_f32_16x16x32_f16 v[34:37], v[176:179], v[220:223], v[34:37]
	v_mfma_f32_16x16x32_f16 v[62:65], v[172:175], v[200:203], v[62:65]
	v_mfma_f32_16x16x32_f16 v[58:61], v[192:195], v[200:203], v[58:61]
	v_mfma_f32_16x16x32_f16 v[54:57], v[172:175], v[208:211], v[54:57]
	v_mfma_f32_16x16x32_f16 v[50:53], v[192:195], v[208:211], v[50:53]
	v_mfma_f32_16x16x32_f16 v[46:49], v[172:175], v[216:219], v[46:49]
	v_mfma_f32_16x16x32_f16 v[42:45], v[192:195], v[216:219], v[42:45]
	v_mfma_f32_16x16x32_f16 v[38:41], v[172:175], v[224:227], v[38:41]
	v_mfma_f32_16x16x32_f16 v[34:37], v[192:195], v[224:227], v[34:37]
	s_setprio 0
	s_barrier
	s_mov_b32 m0, s94
	s_add_u32 s100, s98, s54
	s_addc_u32 s101, s99, s55
	global_load_lds_dwordx4 v254, s[100:101]
	s_mov_b32 m0, s95
	s_nop 0
	global_load_lds_dwordx4 v255, s[100:101]
	s_waitcnt vmcnt(6)
	s_barrier
	s_setprio 1
	v_mfma_f32_16x16x32_f16 v[30:33], v[228:231], v[196:199], v[30:33]
	v_mfma_f32_16x16x32_f16 v[26:29], v[236:239], v[196:199], v[26:29]
	v_mfma_f32_16x16x32_f16 v[22:25], v[228:231], v[204:207], v[22:25]
	v_mfma_f32_16x16x32_f16 v[18:21], v[236:239], v[204:207], v[18:21]
	v_mfma_f32_16x16x32_f16 v[14:17], v[228:231], v[212:215], v[14:17]
	v_mfma_f32_16x16x32_f16 v[10:13], v[236:239], v[212:215], v[10:13]
	v_mfma_f32_16x16x32_f16 v[6:9], v[228:231], v[220:223], v[6:9]
	v_mfma_f32_16x16x32_f16 v[2:5], v[236:239], v[220:223], v[2:5]
	v_mfma_f32_16x16x32_f16 v[30:33], v[232:235], v[200:203], v[30:33]
	v_mfma_f32_16x16x32_f16 v[26:29], v[240:243], v[200:203], v[26:29]
	v_mfma_f32_16x16x32_f16 v[22:25], v[232:235], v[208:211], v[22:25]
	v_mfma_f32_16x16x32_f16 v[18:21], v[240:243], v[208:211], v[18:21]
	v_mfma_f32_16x16x32_f16 v[14:17], v[232:235], v[216:219], v[14:17]
	v_mfma_f32_16x16x32_f16 v[10:13], v[240:243], v[216:219], v[10:13]
	v_mfma_f32_16x16x32_f16 v[6:9], v[232:235], v[224:227], v[6:9]
	v_mfma_f32_16x16x32_f16 v[2:5], v[240:243], v[224:227], v[2:5]
	s_setprio 0
	s_add_i32 s35, s35, 2
	s_add_u32 s96, s96, 0x100
	s_addc_u32 s97, s97, 0
	s_add_u32 s98, s98, 0x100
	s_addc_u32 s99, s99, 0
	s_cmp_lt_u32 s35, 28
	s_barrier
	s_cbranch_scc1 .LBB5_9
	v_add_u32_e32 v143, 0xc000, v142
	s_add_u32 s0, s50, 0x80f80
	v_readfirstlane_b32 s2, v143
	s_addc_u32 s1, s51, 0
	s_mov_b32 m0, s2
	ds_read_b128 v[134:137], v165
	ds_read_b128 v[138:141], v165 offset:1024
	ds_read_b128 v[154:157], v165 offset:2048
	ds_read_b128 v[158:161], v165 offset:3072
	global_load_lds_dwordx4 v130, s[0:1]
	v_add_u32_e32 v130, 0xe000, v142
	s_nop 0
	v_readfirstlane_b32 s2, v130
	s_mov_b32 m0, s2
	s_nop 0
	global_load_lds_dwordx4 v132, s[0:1]
	ds_read_b128 v[142:145], v150
	ds_read_b128 v[166:169], v150 offset:1024
	ds_read_b128 v[170:173], v149
	ds_read_b128 v[174:177], v149 offset:1024
	ds_read_b128 v[192:195], v148
	ds_read_b128 v[196:199], v148 offset:1024
	ds_read_b128 v[200:203], v147
	ds_read_b128 v[204:207], v147 offset:1024
	s_barrier
	s_waitcnt lgkmcnt(0)
	s_setprio 1
	s_waitcnt lgkmcnt(0)
	v_mfma_f32_16x16x32_f16 v[126:129], v[134:137], v[142:145], v[126:129]
	v_mfma_f32_16x16x32_f16 v[122:125], v[154:157], v[142:145], v[122:125]
	v_mfma_f32_16x16x32_f16 v[118:121], v[134:137], v[170:173], v[118:121]
	v_mfma_f32_16x16x32_f16 v[114:117], v[154:157], v[170:173], v[114:117]
	v_mfma_f32_16x16x32_f16 v[110:113], v[134:137], v[192:195], v[110:113]
	v_mfma_f32_16x16x32_f16 v[106:109], v[154:157], v[192:195], v[106:109]
	v_mfma_f32_16x16x32_f16 v[102:105], v[134:137], v[200:203], v[102:105]
	v_mfma_f32_16x16x32_f16 v[98:101], v[154:157], v[200:203], v[98:101]
	v_mfma_f32_16x16x32_f16 v[126:129], v[138:141], v[166:169], v[126:129]
	v_mfma_f32_16x16x32_f16 v[122:125], v[158:161], v[166:169], v[122:125]
	v_mfma_f32_16x16x32_f16 v[118:121], v[138:141], v[174:177], v[118:121]
	v_mfma_f32_16x16x32_f16 v[114:117], v[158:161], v[174:177], v[114:117]
	v_mfma_f32_16x16x32_f16 v[110:113], v[138:141], v[196:199], v[110:113]
	v_mfma_f32_16x16x32_f16 v[106:109], v[158:161], v[196:199], v[106:109]
	v_mfma_f32_16x16x32_f16 v[102:105], v[138:141], v[204:207], v[102:105]
	v_mfma_f32_16x16x32_f16 v[98:101], v[158:161], v[204:207], v[98:101]
	s_setprio 0
	s_barrier
	ds_read_b128 v[208:211], v163
	ds_read_b128 v[212:215], v163 offset:1024
	ds_read_b128 v[216:219], v163 offset:2048
	ds_read_b128 v[220:223], v163 offset:3072
	s_barrier
	s_waitcnt lgkmcnt(0)
	s_setprio 1
	s_waitcnt lgkmcnt(0)
	v_mfma_f32_16x16x32_f16 v[86:89], v[208:211], v[170:173], v[86:89]
	v_mfma_f32_16x16x32_f16 v[82:85], v[216:219], v[170:173], v[82:85]
	v_mfma_f32_16x16x32_f16 v[78:81], v[208:211], v[192:195], v[78:81]
	v_mfma_f32_16x16x32_f16 v[74:77], v[216:219], v[192:195], v[74:77]
	v_mfma_f32_16x16x32_f16 v[70:73], v[208:211], v[200:203], v[70:73]
	v_mfma_f32_16x16x32_f16 v[66:69], v[216:219], v[200:203], v[66:69]
	v_mfma_f32_16x16x32_f16 v[94:97], v[208:211], v[142:145], v[94:97]
	v_mfma_f32_16x16x32_f16 v[90:93], v[216:219], v[142:145], v[90:93]
	v_mfma_f32_16x16x32_f16 v[86:89], v[212:215], v[174:177], v[86:89]
	v_mfma_f32_16x16x32_f16 v[82:85], v[220:223], v[174:177], v[82:85]
	v_mfma_f32_16x16x32_f16 v[78:81], v[212:215], v[196:199], v[78:81]
	v_mfma_f32_16x16x32_f16 v[74:77], v[220:223], v[196:199], v[74:77]
	v_mfma_f32_16x16x32_f16 v[70:73], v[212:215], v[204:207], v[70:73]
	v_mfma_f32_16x16x32_f16 v[66:69], v[220:223], v[204:207], v[66:69]
	v_mfma_f32_16x16x32_f16 v[224:227], v[212:215], v[166:169], v[94:97]
	v_mfma_f32_16x16x32_f16 v[166:169], v[220:223], v[166:169], v[90:93]
	s_setprio 0
	s_barrier
	s_nop 0
	ds_read_b128 v[90:93], v150 offset:16384
	ds_read_b128 v[94:97], v150 offset:17408
	ds_read_b128 v[142:145], v149 offset:16384
	ds_read_b128 v[170:173], v149 offset:17408
	ds_read_b128 v[174:177], v148 offset:16384
	ds_read_b128 v[192:195], v148 offset:17408
	ds_read_b128 v[196:199], v147 offset:16384
	ds_read_b128 v[200:203], v147 offset:17408
	s_waitcnt vmcnt(4)
	s_barrier
	s_waitcnt lgkmcnt(0)
	s_setprio 1
	s_waitcnt lgkmcnt(0)
	v_mfma_f32_16x16x32_f16 v[62:65], v[134:137], v[90:93], v[62:65]
	v_mfma_f32_16x16x32_f16 v[58:61], v[154:157], v[90:93], v[58:61]
	v_mfma_f32_16x16x32_f16 v[54:57], v[134:137], v[142:145], v[54:57]
	v_mfma_f32_16x16x32_f16 v[50:53], v[154:157], v[142:145], v[50:53]
	v_mfma_f32_16x16x32_f16 v[46:49], v[134:137], v[174:177], v[46:49]
	v_mfma_f32_16x16x32_f16 v[42:45], v[154:157], v[174:177], v[42:45]
	v_mfma_f32_16x16x32_f16 v[38:41], v[134:137], v[196:199], v[38:41]
	v_mfma_f32_16x16x32_f16 v[62:65], v[138:141], v[94:97], v[62:65]
	v_mfma_f32_16x16x32_f16 v[58:61], v[158:161], v[94:97], v[58:61]
	v_mfma_f32_16x16x32_f16 v[54:57], v[138:141], v[170:173], v[54:57]
	v_mfma_f32_16x16x32_f16 v[50:53], v[158:161], v[170:173], v[50:53]
	v_mfma_f32_16x16x32_f16 v[46:49], v[138:141], v[192:195], v[46:49]
	v_mfma_f32_16x16x32_f16 v[42:45], v[158:161], v[192:195], v[42:45]
	v_mfma_f32_16x16x32_f16 v[38:41], v[138:141], v[200:203], v[38:41]
	v_mfma_f32_16x16x32_f16 v[34:37], v[154:157], v[196:199], v[34:37]
	v_mfma_f32_16x16x32_f16 v[34:37], v[158:161], v[200:203], v[34:37]
	s_setprio 0
	s_setprio 1
	v_mfma_f32_16x16x32_f16 v[30:33], v[208:211], v[90:93], v[30:33]
	v_mfma_f32_16x16x32_f16 v[6:9], v[208:211], v[196:199], v[6:9]
	v_mfma_f32_16x16x32_f16 v[2:5], v[216:219], v[196:199], v[2:5]
	v_mfma_f32_16x16x32_f16 v[30:33], v[212:215], v[94:97], v[30:33]
	v_mfma_f32_16x16x32_f16 v[26:29], v[216:219], v[90:93], v[26:29]
	v_mfma_f32_16x16x32_f16 v[22:25], v[208:211], v[142:145], v[22:25]
	v_mfma_f32_16x16x32_f16 v[18:21], v[216:219], v[142:145], v[18:21]
	v_mfma_f32_16x16x32_f16 v[14:17], v[208:211], v[174:177], v[14:17]
	v_mfma_f32_16x16x32_f16 v[10:13], v[216:219], v[174:177], v[10:13]
	v_mfma_f32_16x16x32_f16 v[6:9], v[212:215], v[200:203], v[6:9]
	v_mfma_f32_16x16x32_f16 v[2:5], v[220:223], v[200:203], v[2:5]
	v_mfma_f32_16x16x32_f16 v[26:29], v[220:223], v[94:97], v[26:29]
	v_mfma_f32_16x16x32_f16 v[154:157], v[212:215], v[170:173], v[22:25]
	v_mfma_f32_16x16x32_f16 v[18:21], v[220:223], v[170:173], v[18:21]
	v_mfma_f32_16x16x32_f16 v[158:161], v[212:215], v[192:195], v[14:17]
	v_mfma_f32_16x16x32_f16 v[10:13], v[220:223], v[192:195], v[10:13]
	s_setprio 0
	s_barrier
	ds_read_b128 v[14:17], v133
	ds_read_b128 v[22:25], v133 offset:1024
	ds_read_b128 v[170:173], v133 offset:2048
	ds_read_b128 v[174:177], v133 offset:3072
	ds_read_b128 v[192:195], v150 offset:32768
	ds_read_b128 v[196:199], v150 offset:33792
	ds_read_b128 v[200:203], v149 offset:32768
	ds_read_b128 v[204:207], v149 offset:33792
	ds_read_b128 v[208:211], v148 offset:32768
	ds_read_b128 v[212:215], v148 offset:33792
	ds_read_b128 v[216:219], v147 offset:32768
	ds_read_b128 v[220:223], v147 offset:33792
	s_waitcnt vmcnt(2)
	s_barrier
	s_waitcnt lgkmcnt(0)
	s_setprio 1
	s_waitcnt lgkmcnt(0)
	v_mfma_f32_16x16x32_f16 v[90:93], v[14:17], v[192:195], v[126:129]
	v_mfma_f32_16x16x32_f16 v[142:145], v[22:25], v[196:199], v[90:93]
	v_mfma_f32_16x16x32_f16 v[90:93], v[170:173], v[192:195], v[122:125]
	v_mfma_f32_16x16x32_f16 v[138:141], v[174:177], v[196:199], v[90:93]
	v_mfma_f32_16x16x32_f16 v[90:93], v[14:17], v[200:203], v[118:121]
	v_mfma_f32_16x16x32_f16 v[126:129], v[22:25], v[204:207], v[90:93]
	v_mfma_f32_16x16x32_f16 v[90:93], v[170:173], v[200:203], v[114:117]
	v_mfma_f32_16x16x32_f16 v[122:125], v[174:177], v[204:207], v[90:93]
	v_mfma_f32_16x16x32_f16 v[90:93], v[14:17], v[208:211], v[110:113]
	v_mfma_f32_16x16x32_f16 v[110:113], v[22:25], v[212:215], v[90:93]
	v_mfma_f32_16x16x32_f16 v[90:93], v[170:173], v[208:211], v[106:109]
	v_mfma_f32_16x16x32_f16 v[106:109], v[174:177], v[212:215], v[90:93]
	v_mfma_f32_16x16x32_f16 v[90:93], v[14:17], v[216:219], v[102:105]
	v_mfma_f32_16x16x32_f16 v[94:97], v[22:25], v[220:223], v[90:93]
	v_mfma_f32_16x16x32_f16 v[90:93], v[170:173], v[216:219], v[98:101]
	v_mfma_f32_16x16x32_f16 v[90:93], v[174:177], v[220:223], v[90:93]
	s_setprio 0
	s_barrier
	ds_read_b128 v[228:231], v131
	ds_read_b128 v[232:235], v131 offset:1024
	ds_read_b128 v[236:239], v131 offset:2048
	ds_read_b128 v[240:243], v131 offset:3072
	s_waitcnt vmcnt(0)
	s_barrier
	s_waitcnt lgkmcnt(0)
	s_setprio 1
	s_waitcnt lgkmcnt(0)
	v_mfma_f32_16x16x32_f16 v[98:101], v[228:231], v[192:195], v[224:227]
	v_mfma_f32_16x16x32_f16 v[134:137], v[232:235], v[196:199], v[98:101]
	v_mfma_f32_16x16x32_f16 v[98:101], v[236:239], v[192:195], v[166:169]
	v_mfma_f32_16x16x32_f16 v[86:89], v[228:231], v[200:203], v[86:89]
	v_mfma_f32_16x16x32_f16 v[82:85], v[236:239], v[200:203], v[82:85]
	v_mfma_f32_16x16x32_f16 v[78:81], v[228:231], v[208:211], v[78:81]
	v_mfma_f32_16x16x32_f16 v[74:77], v[236:239], v[208:211], v[74:77]
	v_mfma_f32_16x16x32_f16 v[70:73], v[228:231], v[216:219], v[70:73]
	v_mfma_f32_16x16x32_f16 v[66:69], v[236:239], v[216:219], v[66:69]
	v_mfma_f32_16x16x32_f16 v[130:133], v[240:243], v[196:199], v[98:101]
	v_mfma_f32_16x16x32_f16 v[118:121], v[232:235], v[204:207], v[86:89]
	v_mfma_f32_16x16x32_f16 v[114:117], v[240:243], v[204:207], v[82:85]
	v_mfma_f32_16x16x32_f16 v[102:105], v[232:235], v[212:215], v[78:81]
	v_mfma_f32_16x16x32_f16 v[98:101], v[240:243], v[212:215], v[74:77]
	v_mfma_f32_16x16x32_f16 v[86:89], v[232:235], v[220:223], v[70:73]
	v_mfma_f32_16x16x32_f16 v[82:85], v[240:243], v[220:223], v[66:69]
	s_setprio 0
	s_barrier
	s_nop 0
	ds_read_b128 v[66:69], v150 offset:49152
	ds_read_b128 v[166:169], v150 offset:50176
	ds_read_b128 v[192:195], v149 offset:49152
	ds_read_b128 v[196:199], v149 offset:50176
	ds_read_b128 v[200:203], v148 offset:49152
	ds_read_b128 v[148:151], v148 offset:50176
	ds_read_b128 v[204:207], v147 offset:49152
	ds_read_b128 v[208:211], v147 offset:50176
	s_barrier
	s_waitcnt lgkmcnt(0)
	s_setprio 1
	s_waitcnt lgkmcnt(0)
	v_mfma_f32_16x16x32_f16 v[62:65], v[14:17], v[66:69], v[62:65]
	v_mfma_f32_16x16x32_f16 v[54:57], v[14:17], v[192:195], v[54:57]
	v_mfma_f32_16x16x32_f16 v[46:49], v[14:17], v[200:203], v[46:49]
	v_mfma_f32_16x16x32_f16 v[14:17], v[14:17], v[204:207], v[38:41]
	v_mfma_f32_16x16x32_f16 v[78:81], v[22:25], v[166:169], v[62:65]
	v_mfma_f32_16x16x32_f16 v[58:61], v[170:173], v[66:69], v[58:61]
	v_mfma_f32_16x16x32_f16 v[62:65], v[22:25], v[196:199], v[54:57]
	v_mfma_f32_16x16x32_f16 v[50:53], v[170:173], v[192:195], v[50:53]
	v_mfma_f32_16x16x32_f16 v[46:49], v[22:25], v[148:151], v[46:49]
	v_mfma_f32_16x16x32_f16 v[42:45], v[170:173], v[200:203], v[42:45]
	v_mfma_f32_16x16x32_f16 v[22:25], v[22:25], v[208:211], v[14:17]
	v_mfma_f32_16x16x32_f16 v[14:17], v[170:173], v[204:207], v[34:37]
	v_mfma_f32_16x16x32_f16 v[74:77], v[174:177], v[166:169], v[58:61]
	v_mfma_f32_16x16x32_f16 v[58:61], v[174:177], v[196:199], v[50:53]
	v_mfma_f32_16x16x32_f16 v[42:45], v[174:177], v[148:151], v[42:45]
	v_mfma_f32_16x16x32_f16 v[14:17], v[174:177], v[208:211], v[14:17]
	s_setprio 0
	s_setprio 1
	v_mfma_f32_16x16x32_f16 v[26:29], v[236:239], v[66:69], v[26:29]
	v_mfma_f32_16x16x32_f16 v[18:21], v[236:239], v[192:195], v[18:21]
	v_mfma_f32_16x16x32_f16 v[30:33], v[228:231], v[66:69], v[30:33]
	v_mfma_f32_16x16x32_f16 v[66:69], v[240:243], v[166:169], v[26:29]
	v_mfma_f32_16x16x32_f16 v[26:29], v[228:231], v[192:195], v[154:157]
	v_mfma_f32_16x16x32_f16 v[50:53], v[240:243], v[196:199], v[18:21]
	v_mfma_f32_16x16x32_f16 v[18:21], v[228:231], v[200:203], v[158:161]
	v_mfma_f32_16x16x32_f16 v[10:13], v[236:239], v[200:203], v[10:13]
	v_mfma_f32_16x16x32_f16 v[6:9], v[228:231], v[204:207], v[6:9]
	v_mfma_f32_16x16x32_f16 v[2:5], v[236:239], v[204:207], v[2:5]
	v_mfma_f32_16x16x32_f16 v[70:73], v[232:235], v[166:169], v[30:33]
	v_mfma_f32_16x16x32_f16 v[54:57], v[232:235], v[196:199], v[26:29]
	v_mfma_f32_16x16x32_f16 v[38:41], v[232:235], v[148:151], v[18:21]
	v_mfma_f32_16x16x32_f16 v[30:33], v[240:243], v[148:151], v[10:13]
	v_mfma_f32_16x16x32_f16 v[6:9], v[232:235], v[208:211], v[6:9]
	v_mfma_f32_16x16x32_f16 v[2:5], v[240:243], v[208:211], v[2:5]
	s_setprio 0
	s_movk_i32 s0, 0x100
	v_cmp_gt_u32_e32 vcc, s0, v0
	s_barrier
	s_and_saveexec_b64 s[0:1], vcc
	s_cbranch_execz .LBB5_12
	s_barrier
